# speedup vs baseline: 1.0036x; 1.0036x over previous
.Lk1_nbx7:
.Lk1_nb_done:
	s_lshl_b32 s32, s24, 6
	s_add_u32 s40, s12, s32
	s_addc_u32 s41, s13, 0
	s_lshl_b32 s32, s24, 4
	s_add_u32 s42, s14, s32
	s_addc_u32 s43, s15, 0
	v_lshlrev_b32_e32 v47, 3, v1
	v_lshlrev_b32_e32 v48, 1, v1
	s_mov_b64 exec, 0xff
	global_store_dwordx2 v47, v[44:45], s[40:41]
	global_store_short v48, v46, s[42:43]
	s_mov_b64 exec, -1
	s_load_dwordx4 s[8:11], s[0:1], 0x18
	s_load_dwordx2 s[12:13], s[0:1], 0x28
	s_load_dwordx4 s[16:19], s[0:1], 0x40
	s_mov_b32 s40, 0x652b82fe
	s_mov_b32 s41, 0x3ff71547
	s_mov_b32 s42, 0xfee00000
	s_mov_b32 s43, 0xbfe62e42
	s_mov_b32 s44, 0x35793c76
	s_mov_b32 s45, 0xbdea39ef
	s_mov_b32 s46, 0xb7789f5c
	s_mov_b32 s47, 0x3e927e4f
	s_mov_b32 s48, 0xa556c734
	s_mov_b32 s49, 0x3ec71de3
	s_mov_b32 s50, 0x1a01a01a
	s_mov_b32 s51, 0x3efa01a0
	s_mov_b32 s52, 0x1a01a01a
	s_mov_b32 s53, 0x3f2a01a0
	s_mov_b32 s54, 0x16c16c17
	s_mov_b32 s55, 0x3f56c16c
	s_mov_b32 s56, 0x11111111
	s_mov_b32 s57, 0x3f811111
	s_mov_b32 s58, 0x55555555
	s_mov_b32 s59, 0x3fa55555
	s_mov_b32 s60, 0x55555555
	s_mov_b32 s61, 0x3fc55555
	v_mov_b32_e32 v44, 0x67f544e4
	v_mov_b32_e32 v45, 0x3e5ae645
	s_mov_b32 s62, 0xfefa39ef
	s_mov_b32 s63, 0x3fe62e42
	s_waitcnt vmcnt(2)
	v_readlane_b32 s64, v16, 0
	v_readlane_b32 s65, v17, 0
	v_readlane_b32 s66, v18, 0
	v_readlane_b32 s67, v19, 0
	s_cmp_eq_u32 s35, 1
	s_cselect_b32 s64, s65, s64
	s_cmp_eq_u32 s35, 2
	s_cselect_b32 s64, s66, s64
	s_cmp_eq_u32 s35, 3
	s_cselect_b32 s36, s67, s64
	s_cmp_le_u32 0, s35
	s_cselect_b64 s[32:33], 1, 0
	v_cndmask_b32_e64 v16, v16, v15, s[32:33]
	s_cmp_le_u32 1, s35
	s_cselect_b64 s[32:33], 1, 0
	v_cndmask_b32_e64 v17, v17, v15, s[32:33]
	s_cmp_le_u32 2, s35
	s_cselect_b64 s[32:33], 1, 0
	v_cndmask_b32_e64 v18, v18, v15, s[32:33]
	s_cmp_le_u32 3, s35
	s_cselect_b64 s[32:33], 1, 0
	v_cndmask_b32_e64 v19, v19, v15, s[32:33]
	s_cmp_lt_u32 s35, 1
	s_cselect_b64 s[32:33], 0x10000, 0
	v_cndmask_b32_e64 v41, v41, v15, s[32:33]
	s_cmp_lt_u32 s35, 2
	s_cselect_b64 s[32:33], 0x10000, 0
	v_cndmask_b32_e64 v42, v42, v15, s[32:33]
	s_cmp_lt_u32 s35, 3
	s_cselect_b64 s[32:33], 0x10000, 0
	v_cndmask_b32_e64 v43, v43, v15, s[32:33]
	v_max3_f32 v52, v16, v17, v18
	v_max3_f32 v53, v19, v20, v21
	v_max3_f32 v52, v52, v22, v23
	v_max3_f32 v53, v53, v24, v25
	v_max3_f32 v52, v52, v26, v27
	v_max3_f32 v52, v52, v28, v29
	v_max3_f32 v53, v53, v30, v31
	v_max3_f32 v52, v52, v32, v33
	v_max3_f32 v52, v52, v34, v35
	v_max3_f32 v53, v53, v36, v37
	v_max3_f32 v52, v52, v38, v39
	v_max3_f32 v53, v53, v40, v41
	v_max3_f32 v52, v52, v42, v43
	v_max_f32_e32 v52, v52, v53
	s_nop 1
	v_max_f32_dpp v52, v52, v52 quad_perm:[1,0,3,2] row_mask:0xf bank_mask:0xf
	s_nop 1
	v_max_f32_dpp v52, v52, v52 quad_perm:[2,3,0,1] row_mask:0xf bank_mask:0xf
	s_nop 1
	v_max_f32_dpp v52, v52, v52 row_half_mirror row_mask:0xf bank_mask:0xf
	s_nop 1
	v_max_f32_dpp v52, v52, v52 row_mirror row_mask:0xf bank_mask:0xf
	s_nop 1
	v_max_f32_dpp v52, v52, v52 row_bcast:15 row_mask:0xa bank_mask:0xf
	s_nop 1
	v_max_f32_dpp v52, v52, v52 row_bcast:31 row_mask:0xc bank_mask:0xf
	s_nop 1
	v_readlane_b32 s28, v52, 63
	v_mov_b32_e32 v53, s36
	v_mov_b32_e32 v56, 0x3fb8aa3b
	v_mov_b32_e32 v57, 0x3fb8aa3b
	v_max_f32_e32 v53, s28, v53
	v_mul_f32_e32 v58, 0xbfb8aa3b, v53
	v_mov_b32_e32 v6, 0
	v_mov_b32_e32 v7, 0
	v_mov_b32_e32 v59, v58
	v_pk_fma_f32 v[60:61], v[16:17], v[56:57], v[58:59]
	v_pk_fma_f32 v[62:63], v[18:19], v[56:57], v[58:59]
	v_exp_f32_e32 v60, v60
	v_exp_f32_e32 v61, v61
	v_exp_f32_e32 v62, v62
	v_exp_f32_e32 v63, v63
	v_pk_fma_f32 v[48:49], v[20:21], v[56:57], v[58:59]
	v_pk_fma_f32 v[50:51], v[22:23], v[56:57], v[58:59]
	v_pk_add_f32 v[60:61], v[60:61], v[62:63]
	s_nop 0
	v_add_f32_e32 v60, v60, v61
	v_cvt_f64_f32_e32 v[4:5], v60
	v_add_f64 v[6:7], v[6:7], v[4:5]
	v_exp_f32_e32 v48, v48
	v_exp_f32_e32 v49, v49
	v_exp_f32_e32 v50, v50
	v_exp_f32_e32 v51, v51
	v_pk_fma_f32 v[60:61], v[24:25], v[56:57], v[58:59]
	v_pk_fma_f32 v[62:63], v[26:27], v[56:57], v[58:59]
	v_pk_add_f32 v[48:49], v[48:49], v[50:51]
	s_nop 0
	v_add_f32_e32 v48, v48, v49
	v_cvt_f64_f32_e32 v[4:5], v48
	v_add_f64 v[6:7], v[6:7], v[4:5]
	v_exp_f32_e32 v60, v60
	v_exp_f32_e32 v61, v61
	v_exp_f32_e32 v62, v62
	v_exp_f32_e32 v63, v63
	v_pk_fma_f32 v[48:49], v[28:29], v[56:57], v[58:59]
	v_pk_fma_f32 v[50:51], v[30:31], v[56:57], v[58:59]
	v_pk_add_f32 v[60:61], v[60:61], v[62:63]
	s_nop 0
	v_add_f32_e32 v60, v60, v61
	v_cvt_f64_f32_e32 v[4:5], v60
	v_add_f64 v[6:7], v[6:7], v[4:5]
	v_exp_f32_e32 v48, v48
	v_exp_f32_e32 v49, v49
	v_exp_f32_e32 v50, v50
	v_exp_f32_e32 v51, v51
	v_pk_fma_f32 v[60:61], v[32:33], v[56:57], v[58:59]
	v_pk_fma_f32 v[62:63], v[34:35], v[56:57], v[58:59]
	v_pk_add_f32 v[48:49], v[48:49], v[50:51]
	s_nop 0
	v_add_f32_e32 v48, v48, v49
	v_cvt_f64_f32_e32 v[4:5], v48
	v_add_f64 v[6:7], v[6:7], v[4:5]
	v_exp_f32_e32 v60, v60
	v_exp_f32_e32 v61, v61
	v_exp_f32_e32 v62, v62
	v_exp_f32_e32 v63, v63
	v_pk_fma_f32 v[48:49], v[36:37], v[56:57], v[58:59]
	v_pk_fma_f32 v[50:51], v[38:39], v[56:57], v[58:59]
	v_pk_add_f32 v[60:61], v[60:61], v[62:63]
	s_nop 0
	v_add_f32_e32 v60, v60, v61
	v_cvt_f64_f32_e32 v[4:5], v60
	v_add_f64 v[6:7], v[6:7], v[4:5]
	v_exp_f32_e32 v48, v48
	v_exp_f32_e32 v49, v49
	v_exp_f32_e32 v50, v50
	v_exp_f32_e32 v51, v51
	v_pk_fma_f32 v[60:61], v[40:41], v[56:57], v[58:59]
	v_pk_fma_f32 v[62:63], v[42:43], v[56:57], v[58:59]
	v_pk_add_f32 v[48:49], v[48:49], v[50:51]
	s_nop 0
	v_add_f32_e32 v48, v48, v49
	v_cvt_f64_f32_e32 v[4:5], v48
	v_add_f64 v[6:7], v[6:7], v[4:5]
	v_exp_f32_e32 v60, v60
	v_exp_f32_e32 v61, v61
	v_exp_f32_e32 v62, v62
	v_exp_f32_e32 v63, v63
	s_nop 0
	v_pk_add_f32 v[60:61], v[60:61], v[62:63]
	s_nop 0
	v_add_f32_e32 v60, v60, v61
	v_cvt_f64_f32_e32 v[4:5], v60
	v_add_f64 v[6:7], v[6:7], v[4:5]
	v_mov_b32_e32 v60, s36
	v_fmamk_f32 v60, v60, 0x3fb8aa3b, v58
	v_exp_f32_e32 v60, v60
	s_nop 1
	v_mov_b32_dpp v4, v6 quad_perm:[1,0,3,2] row_mask:0xf bank_mask:0xf
	v_mov_b32_dpp v5, v7 quad_perm:[1,0,3,2] row_mask:0xf bank_mask:0xf
	v_add_f64 v[6:7], v[6:7], v[4:5]
	s_nop 1
	v_mov_b32_dpp v4, v6 quad_perm:[2,3,0,1] row_mask:0xf bank_mask:0xf
	v_mov_b32_dpp v5, v7 quad_perm:[2,3,0,1] row_mask:0xf bank_mask:0xf
	v_add_f64 v[6:7], v[6:7], v[4:5]
	s_nop 1
	v_mov_b32_dpp v4, v6 row_half_mirror row_mask:0xf bank_mask:0xf
	v_mov_b32_dpp v5, v7 row_half_mirror row_mask:0xf bank_mask:0xf
	v_add_f64 v[6:7], v[6:7], v[4:5]
	s_nop 1
	v_mov_b32_dpp v4, v6 row_mirror row_mask:0xf bank_mask:0xf
	v_mov_b32_dpp v5, v7 row_mirror row_mask:0xf bank_mask:0xf
	v_add_f64 v[6:7], v[6:7], v[4:5]
	v_cvt_f64_f32_e32 v[8:9], v60
	v_readlane_b32 s64, v6, 15
	v_readlane_b32 s65, v7, 15
	v_readlane_b32 s66, v6, 31
	v_readlane_b32 s67, v7, 31
	v_readlane_b32 s68, v6, 47
	v_readlane_b32 s69, v7, 47
	v_readlane_b32 s70, v6, 63
	v_readlane_b32 s71, v7, 63
	v_add_f64 v[6:7], s[64:65], 0
	v_add_f64 v[6:7], v[6:7], s[66:67]
	v_add_f64 v[6:7], v[6:7], s[68:69]
	v_add_f64 v[6:7], v[6:7], s[70:71]
	v_add_f64 v[6:7], v[6:7], v[8:9]
	s_mov_b32 s29, 1
	s_mov_b32 s31, 1
	s_mov_b32 s30, 0xff800000
	s_cmp_eq_u32 s27, 0
	s_cbranch_scc1 .Lk1_lse
	s_mov_b32 s37, 0x7fffffff
	v_cmp_eq_f32_e64 s[64:65], s28, v16
	v_cmp_eq_f32_e64 s[66:67], s28, v17
	v_cmp_eq_f32_e64 s[68:69], s28, v18
	v_cmp_eq_f32_e64 s[70:71], s28, v19
	s_or_b64 s[32:33], s[64:65], s[66:67]
	s_or_b64 s[72:73], s[68:69], s[70:71]
	s_or_b64 s[32:33], s[32:33], s[72:73]
	s_cmp_eq_u64 s[32:33], 0
	s_cbranch_scc1 .Lk1_a1_n0
	s_ff1_i32_b64 s32, s[64:65]
	s_lshl_b32 s33, s32, 2
	s_cmp_lt_i32 s32, 0
	s_cselect_b32 s33, 0x7fffffff, s33
	s_min_u32 s37, s37, s33
	s_ff1_i32_b64 s32, s[66:67]
	s_lshl_b32 s33, s32, 2
	s_add_u32 s33, s33, 1
	s_cmp_lt_i32 s32, 0
	s_cselect_b32 s33, 0x7fffffff, s33
	s_min_u32 s37, s37, s33
	s_ff1_i32_b64 s32, s[68:69]
	s_lshl_b32 s33, s32, 2
	s_add_u32 s33, s33, 2
	s_cmp_lt_i32 s32, 0
	s_cselect_b32 s33, 0x7fffffff, s33
	s_min_u32 s37, s37, s33
	s_ff1_i32_b64 s32, s[70:71]
	s_lshl_b32 s33, s32, 2
	s_add_u32 s33, s33, 3
	s_cmp_lt_i32 s32, 0
	s_cselect_b32 s33, 0x7fffffff, s33
	s_min_u32 s37, s37, s33
	s_lshr_b32 s32, s37, 2
	s_and_b32 s33, s37, 3
	s_lshl_b64 s[72:73], 1, s32
	s_cmp_eq_u32 s33, 0
	s_cselect_b64 s[64:65], s[72:73], 0
	v_cndmask_b32_e64 v16, v16, v15, s[64:65]
	s_cmp_eq_u32 s33, 1
	s_cselect_b64 s[64:65], s[72:73], 0
	v_cndmask_b32_e64 v17, v17, v15, s[64:65]
	s_cmp_eq_u32 s33, 2
	s_cselect_b64 s[64:65], s[72:73], 0
	v_cndmask_b32_e64 v18, v18, v15, s[64:65]
	s_cmp_eq_u32 s33, 3
	s_cselect_b64 s[64:65], s[72:73], 0
	v_cndmask_b32_e64 v19, v19, v15, s[64:65]
	s_sub_u32 s37, s37, s35
	s_branch .Lk1_a1_done
